# cache-policy: row pass A layer-0 input loads and router row pass X loads non-temporal
# speedup vs baseline: 1.0060x; 1.0060x over previous
.LBB0_378:
	s_or_b64 exec, exec, s[12:13]
	v_ashrrev_i32_e32 v39, 31, v38
	v_lshl_add_u64 v[38:39], v[38:39], 3, s[0:1]
	global_load_dwordx2 v[38:39], v[38:39], off
	v_ashrrev_i32_e32 v63, 31, v62
	v_lshlrev_b64 v[36:37], v36, v[62:63]
	v_lshlrev_b64 v[34:35], 12, v[34:35]
	s_waitcnt vmcnt(0)
	v_lshl_add_u64 v[36:37], v[38:39], 0, v[36:37]
	v_lshl_add_u64 v[34:35], v[36:37], 0, v[34:35]
	v_lshl_add_u64 v[34:35], v[34:35], 0, v[0:1]
	global_load_dwordx4 v[70:73], v[34:35], off nt
	global_load_dwordx4 v[58:61], v[34:35], off offset:1024 nt
	global_load_dwordx4 v[54:57], v[34:35], off offset:2048 nt
	global_load_dwordx4 v[42:45], v[34:35], off offset:3072 nt

.LBB0_388:
	s_or_b64 exec, exec, s[14:15]
	v_ashrrev_i32_e32 v37, 31, v36
	v_lshl_add_u64 v[36:37], v[36:37], 3, s[0:1]
	global_load_dwordx2 v[36:37], v[36:37], off
	v_ashrrev_i32_e32 v65, 31, v64
	v_lshlrev_b64 v[34:35], v34, v[64:65]
	v_lshlrev_b64 v[38:39], 12, v[66:67]
	s_waitcnt vmcnt(0)
	v_lshl_add_u64 v[34:35], v[36:37], 0, v[34:35]
	v_lshl_add_u64 v[34:35], v[34:35], 0, v[38:39]
	v_lshl_add_u64 v[34:35], v[34:35], 0, v[0:1]
	global_load_dwordx4 v[50:53], v[34:35], off nt
	global_load_dwordx4 v[46:49], v[34:35], off offset:1024 nt
	global_load_dwordx4 v[38:41], v[34:35], off offset:2048 nt
	s_nop 0
	global_load_dwordx4 v[34:37], v[34:35], off offset:3072 nt
	v_cndmask_b32_e64 v99, 8, v64, s[12:13]
	v_cndmask_b32_e64 v100, 8, v62, s[10:11]
	s_and_b64 vcc, exec, s[90:91]
	s_cbranch_vccnz .LBB0_382

.LBB0_1534:
	s_mul_i32 s6, s73, 10
	s_add_i32 s20, s6, 7
	s_movk_i32 s6, 0x48
	s_ashr_i32 s7, s6, 31
	s_lshl_b64 s[6:7], s[6:7], 2
	s_add_u32 s6, s0, s6
	s_addc_u32 s7, s1, s7
	s_load_dwordx2 s[8:9], s[6:7], 0x0
	s_waitcnt lgkmcnt(0)
	s_cmp_le_i32 s8, s20
	s_cselect_b64 s[6:7], -1, 0
	s_cmp_lt_i32 s20, s9
	s_cselect_b64 s[8:9], -1, 0
	s_and_b64 s[6:7], s[6:7], s[8:9]
	s_andn2_b64 vcc, exec, s[6:7]
	s_cbranch_vccnz .LBB0_1613
	v_mbcnt_lo_u32_b32 v74, -1, 0
	v_mbcnt_hi_u32_b32 v74, -1, v74
	s_getreg_b32 s6, hwreg(HW_REG_HW_ID, 0, 6)
	s_lshl_b32 s6, s6, 2
	s_and_b32 s6, s6, 0xfc
	s_or_b32 s6, s6, 0x27100
	v_mov_b32_e32 v0, s6
	ds_read_b32 v0, v0
	s_waitcnt vmcnt(0) lgkmcnt(0)
	s_barrier
	v_readfirstlane_b32 s6, v0
	s_nop 1
	v_lshl_or_b32 v138, s6, 6, v74
	v_cmp_gt_i32_e64 s[6:7], 32, v138
	v_readfirstlane_b32 s10, v138
	v_lshl_add_u32 v146, v138, 2, 0
	s_and_saveexec_b64 s[8:9], s[6:7]
	v_add_u32_e32 v0, 0x20000, v146
	ds_write_b32 v0, v1
	s_or_b64 exec, exec, s[8:9]
	s_and_b64 s[8:9], s[4:5], exec
	s_movk_i32 s8, 0x880
	s_cselect_b32 s11, s8, 0x800
	s_mov_b32 s8, 35
	s_ashr_i32 s9, s8, 31
	s_ashr_i32 s16, s10, 6
	s_lshl_b64 s[8:9], s[8:9], 3
	s_add_u32 s8, s0, s8
	s_addc_u32 s9, s1, s9
	s_load_dwordx2 s[8:9], s[8:9], 0x0
	v_readlane_b32 s10, v254, 38
	s_mul_hi_u32 s10, s11, s10
	v_readlane_b32 s15, v254, 39
	s_mul_i32 s12, s10, s15
	s_waitcnt lgkmcnt(0)
	s_add_u32 s8, s8, 0x1a800000
	s_addc_u32 s9, s9, 0
	s_sub_i32 s12, s11, s12
	s_add_i32 s13, s10, 1
	s_sub_i32 s14, s12, s15
	s_cmp_ge_u32 s12, s15
	s_cselect_b32 s10, s13, s10
	s_cselect_b32 s12, s14, s12
	s_add_i32 s13, s10, 1
	s_cmp_ge_u32 s12, s15
	s_cselect_b32 s10, s13, s10
	v_readlane_b32 s12, v254, 40
	s_xor_b32 s10, s10, s12
	s_sub_i32 s17, s10, s12
	s_mul_i32 s10, s17, s3
	s_sub_i32 s12, s11, s10
	s_cmp_lt_i32 s2, s12
	s_cselect_b64 s[10:11], -1, 0
	s_min_i32 s18, s2, s12
	s_cmp_lg_u64 s[10:11], 0
	s_addc_u32 s21, s17, 0
	v_and_b32_e32 v147, 63, v74
	s_cmp_gt_i32 s21, 0
	s_cselect_b64 s[14:15], -1, 0
	s_cmp_lt_i32 s21, 1
	v_lshlrev_b32_e32 v72, 5, v147
	s_cbranch_scc1 .LBB0_1539
	s_mul_i32 s10, s17, s2
	s_add_i32 s10, s18, s10
	s_lshl_b32 s10, s10, 4
	s_lshl_b32 s11, s16, 1
	s_add_i32 s12, s10, s11
	s_ashr_i32 s10, s12, 12
	s_mulk_i32 s10, 0x1100
	s_and_b32 s11, s12, 0xffe
	s_add_i32 s13, s10, s11
	s_and_b64 s[10:11], s[4:5], exec
	s_cselect_b32 s10, s12, s13
	s_ashr_i32 s11, s10, 31
	s_lshl_b64 s[10:11], s[10:11], 11
	s_add_u32 s10, s8, s10
	s_addc_u32 s11, s9, s11
	global_load_dwordx4 v[126:129], v72, s[10:11] offset:16 nt
	global_load_dwordx4 v[134:137], v72, s[10:11] nt
	global_load_dwordx4 v[122:125], v72, s[10:11] offset:2064 nt
	global_load_dwordx4 v[130:133], v72, s[10:11] offset:2048 nt

.LBB0_1545:
	s_add_i32 s27, s27, 1
	v_mov_b64_e32 v[110:111], v[134:135]
	v_mov_b64_e32 v[106:107], v[126:127]
	v_mov_b64_e32 v[118:119], v[130:131]
	v_mov_b64_e32 v[114:115], v[122:123]
	s_cmp_ge_i32 s27, s21
	v_mov_b64_e32 v[112:113], v[136:137]
	v_mov_b64_e32 v[108:109], v[128:129]
	v_mov_b64_e32 v[120:121], v[132:133]
	v_mov_b64_e32 v[116:117], v[124:125]
	s_cbranch_scc1 .LBB0_1547
	s_add_i32 s14, s26, 16
	s_ashr_i32 s12, s14, 12
	s_mulk_i32 s12, 0x1100
	s_and_b32 s13, s14, 0xffe
	s_add_i32 s15, s12, s13
	s_and_b64 s[12:13], s[4:5], exec
	s_cselect_b32 s12, s14, s15
	s_ashr_i32 s13, s12, 31
	s_lshl_b64 s[12:13], s[12:13], 11
	v_lshl_add_u64 v[118:119], v[140:141], 0, s[12:13]
	global_load_dwordx4 v[106:109], v[118:119], off offset:16 nt
	global_load_dwordx4 v[110:113], v[118:119], off nt
	global_load_dwordx4 v[114:117], v[118:119], off offset:2064 nt
	s_nop 0
	global_load_dwordx4 v[118:121], v[118:119], off offset:2048 nt
